# ATT0 tile loop: QK MFMAs interleaved with softmax-finish VALU and PV MFMAs with softmax-start VALU inside each wave; V tile keys staged in natural order so the 8 permlane32 swaps per tile are dropped
# baseline (speedup 1.0000x reference)
.LBB0_502:
	v_mul_f32_e32 v0, v96, v0
	v_mul_f32_e32 v1, v96, v1
	v_mul_f32_e32 v21, v96, v21
	v_mul_f32_e32 v0, v0, v157
	v_mul_f32_e32 v1, v1, v156
	v_mul_f32_e32 v21, v21, v143
	v_med3_f32 v0, v0, s70, v178
	v_med3_f32 v1, v1, s70, v178
	v_mov_b32_e32 v143, v153
	v_cvt_pk_fp8_f32 v143, v0, v1
	v_mul_f32_e32 v2, v96, v2
	v_mul_f32_e32 v3, v96, v3
	v_mul_f32_e32 v2, v2, v155
	v_mul_f32_e32 v3, v3, v154
	v_mul_f32_e32 v20, v96, v20
	v_med3_f32 v0, v2, s70, v178
	v_med3_f32 v1, v3, s70, v178
	v_mul_f32_e32 v20, v20, v144
	v_mul_f32_e32 v10, v96, v10
	v_cvt_pk_fp8_f32 v143, v0, v1 op_sel:[0,0,1]
	v_med3_f32 v0, v94, s70, v178
	v_med3_f32 v1, v95, s70, v178
	v_mov_b32_e32 v144, v153
	v_mul_f32_e32 v10, v10, v145
	v_cvt_pk_fp8_f32 v144, v0, v1
	v_med3_f32 v0, v90, s70, v178
	v_med3_f32 v1, v91, s70, v178
	v_mov_b32_e32 v145, v153
	v_cvt_pk_fp8_f32 v145, v0, v1
	v_mul_f32_e32 v9, v96, v9
	v_med3_f32 v0, v88, s70, v178
	v_med3_f32 v1, v89, s70, v178
	v_mul_f32_e32 v8, v96, v8
	v_mul_f32_e32 v9, v9, v146
	v_cvt_pk_fp8_f32 v145, v0, v1 op_sel:[0,0,1]
	v_med3_f32 v0, v86, s70, v178
	v_med3_f32 v1, v87, s70, v178
	v_mov_b32_e32 v146, v153
	v_mul_f32_e32 v8, v8, v147
	v_cvt_pk_fp8_f32 v146, v0, v1
	v_med3_f32 v0, v82, s70, v178
	v_med3_f32 v1, v83, s70, v178
	v_mov_b32_e32 v147, v153
	v_cvt_pk_fp8_f32 v147, v0, v1
	v_mul_f32_e32 v5, v96, v5
	v_mul_f32_e32 v5, v5, v182
	v_med3_f32 v0, v80, s70, v178
	v_med3_f32 v1, v81, s70, v178
	v_lshlrev_b32_e32 v182, 4, v180
	v_cvt_pk_fp8_f32 v147, v0, v1 op_sel:[0,0,1]
	v_add_u32_e32 v0, s80, v182
	v_ashrrev_i32_e32 v1, 31, v0
	v_med3_f32 v2, v92, s70, v178
	v_med3_f32 v3, v93, s70, v178
	v_add_u32_sdwa v1, v0, v1 dst_sel:DWORD dst_unused:UNUSED_PAD src0_sel:DWORD src1_sel:BYTE_3
	v_cvt_pk_fp8_f32 v144, v2, v3 op_sel:[0,0,1]
	v_med3_f32 v2, v84, s70, v178
	v_med3_f32 v3, v85, s70, v178
	v_ashrrev_i32_e32 v1, 8, v1
	v_cvt_pk_fp8_f32 v146, v2, v3 op_sel:[0,0,1]
	v_mul_i32_i24_e32 v2, 0x100, v1
	v_sub_u32_e32 v2, v0, v2
	v_ashrrev_i32_e32 v2, 4, v2
	v_bitop3_b32 v2, v2, v1, 15 bitop3:0x78
	v_lshlrev_b32_e32 v3, 4, v2
	v_cmp_gt_i32_e32 vcc, 12, v2
	v_mul_f32_e32 v11, v96, v11
	v_mul_f32_e32 v11, v11, v152
	v_cndmask_b32_e32 v2, 0, v3, vcc
	v_mad_i32_i24 v152, v1, s88, v2
	v_add_u32_e32 v1, 0x2000, v0
	v_ashrrev_i32_e32 v2, 31, v1
	v_add_u32_sdwa v2, v1, v2 dst_sel:DWORD dst_unused:UNUSED_PAD src0_sel:DWORD src1_sel:BYTE_3
	s_mul_i32 s5, s6, 0x6c0000
	v_ashrrev_i32_e32 v2, 8, v2
	s_mul_hi_i32 s4, s6, 0x6c0000
	s_add_u32 s5, s68, s5
	v_mul_i32_i24_e32 v3, 0x100, v2
	s_addc_u32 s4, s69, s4
	v_mul_f32_e32 v4, v96, v4
	v_sub_u32_e32 v3, v1, v3
	s_add_u32 s64, s5, s7
	v_mul_f32_e32 v22, v96, v22
	v_mul_f32_e32 v4, v4, v184
	v_ashrrev_i32_e32 v3, 4, v3
	s_addc_u32 s65, s4, 0
	s_mul_i32 s5, s6, 0x1200000
	v_mul_f32_e32 v22, v22, v142
	v_med3_f32 v4, v4, s70, v178
	v_med3_f32 v5, v5, s70, v178
	v_mov_b32_e32 v142, v153
	v_bitop3_b32 v3, v3, v2, 15 bitop3:0x78
	s_mul_hi_i32 s4, s6, 0x1200000
	s_add_u32 s5, s12, s5
	v_cvt_pk_fp8_f32 v142, v4, v5
	v_lshlrev_b32_e32 v4, 4, v3
	v_cmp_gt_i32_e32 vcc, 12, v3
	s_addc_u32 s6, s13, s4
	s_lshl_b32 s4, s59, 9
	v_cndmask_b32_e32 v3, 0, v4, vcc
	s_add_u32 s4, s5, s4
	v_mul_f32_e32 v48, v48, v96
	v_mul_f32_e32 v49, v49, v96
	v_mad_i32_i24 v154, v2, s88, v3
	v_bfe_u32 v2, v180, 2, 2
	v_lshrrev_b32_e32 v4, 2, v180
	s_addc_u32 s5, s6, 0
	v_mul_f32_e32 v48, v48, v108
	v_mul_f32_e32 v49, v49, v107
	v_mul_f32_e32 v25, v96, v25
	v_and_b32_e32 v3, 48, v182
	v_and_or_b32 v2, v4, 4, v2
	v_ashrrev_i32_e32 v4, 8, v0
	v_lshrrev_b32_e32 v0, 3, v0
	s_movk_i32 s6, 0xc0
	v_mul_f32_e32 v25, v25, v131
	v_med3_f32 v48, v48, s70, v178
	v_med3_f32 v49, v49, s70, v178
	v_mov_b32_e32 v131, v153
	v_and_or_b32 v0, v0, s6, v3
	v_and_b32_e32 v3, 0x7fff0, v4
	s_nop 0
	s_add_u32 s66, s4, 0x58200100
	v_mul_f32_e32 v23, v96, v23
	v_cvt_pk_fp8_f32 v131, v48, v49
	v_and_b32_e32 v4, 8, v4
	s_addc_u32 s67, s5, 0
	v_mul_f32_e32 v50, v50, v96
	v_mul_f32_e32 v51, v51, v96
	v_mul_f32_e32 v23, v23, v141
	v_med3_f32 v8, v8, s70, v178
	v_med3_f32 v9, v9, s70, v178
	v_mov_b32_e32 v141, v153
	v_or3_b32 v3, v3, v4, v2
	v_ashrrev_i32_e32 v1, 8, v1
	s_add_i32 s56, s80, 0
	v_mul_f32_e32 v50, v50, v106
	v_mul_f32_e32 v51, v51, v105
	v_cvt_pk_fp8_f32 v141, v8, v9
	v_lshl_or_b32 v156, v3, 13, v0
	v_and_b32_e32 v3, 0x7fff0, v1
	s_nop 0
	s_add_i32 s57, s56, 0x8000
	s_add_i32 s86, s56, 0xa000
	v_ashrrev_i32_e32 v183, 5, v180
	v_med3_f32 v48, v50, s70, v178
	v_med3_f32 v49, v51, s70, v178
	v_and_b32_e32 v1, 8, v1
	s_mov_b32 m0, s57
	s_cmp_lg_u32 0, -1
	v_mul_f32_e32 v7, v96, v7
	v_cvt_pk_fp8_f32 v131, v48, v49 op_sel:[0,0,1]
	v_or3_b32 v1, v3, v1, v2
	global_load_lds_dwordx4 v152, s[64:65]
	s_mov_b32 m0, s86
	s_cselect_b32 s6, 0, 0
	s_add_i32 s91, s56, 0x2000
	v_lshlrev_b32_e32 v48, 1, v183
	v_mul_f32_e32 v7, v7, v158
	v_med3_f32 v8, v10, s70, v178
	v_med3_f32 v9, v11, s70, v178
	v_lshl_or_b32 v158, v1, 13, v0
	global_load_lds_dwordx4 v154, s[64:65]
	s_mov_b32 m0, s56
	s_add_u32 s38, s64, 0x30000
	v_bitop3_b32 v0, v48, v180, 15 bitop3:0x78
	v_cvt_pk_fp8_f32 v141, v8, v9 op_sel:[0,0,1]
	global_load_lds_dwordx4 v156, s[66:67]
	s_mov_b32 m0, s91
	s_addc_u32 s39, s65, 0
	s_add_i32 s95, s56, 0xc000
	v_lshlrev_b32_e32 v49, 8, v181
	v_lshlrev_b32_e32 v8, 4, v0
	v_mul_f32_e32 v6, v96, v6
	global_load_lds_dwordx4 v158, s[66:67]
	s_mov_b32 m0, s95
	s_add_i32 s18, s56, 0xe000
	v_add_u32_e32 v4, v8, v49
	v_mul_f32_e32 v60, v60, v96
	v_mul_f32_e32 v61, v61, v96
	v_mul_f32_e32 v56, v56, v96
	v_mul_f32_e32 v57, v57, v96
	v_mul_f32_e32 v52, v52, v96
	v_mul_f32_e32 v53, v53, v96
	v_mul_f32_e32 v44, v96, v44
	v_mul_f32_e32 v45, v96, v45
	v_mul_f32_e32 v40, v96, v40
	v_mul_f32_e32 v41, v96, v41
	v_mul_f32_e32 v36, v96, v36
	v_mul_f32_e32 v37, v96, v37
	v_mul_f32_e32 v32, v96, v32
	v_mul_f32_e32 v33, v96, v33
	v_mul_f32_e32 v6, v6, v159
	global_load_lds_dwordx4 v152, s[38:39]
	s_mov_b32 m0, s18
	v_add_u32_e32 v184, 0, v4
	v_xor_b32_e32 v4, 16, v4
	v_mul_f32_e32 v60, v60, v104
	v_mul_f32_e32 v61, v61, v103
	v_mul_f32_e32 v56, v56, v100
	v_mul_f32_e32 v57, v57, v99
	v_mul_f32_e32 v52, v52, v112
	v_mul_f32_e32 v53, v53, v111
	v_mul_f32_e32 v44, v44, v120
	v_mul_f32_e32 v45, v45, v119
	v_mul_f32_e32 v40, v40, v116
	v_mul_f32_e32 v41, v41, v115
	v_mul_f32_e32 v36, v36, v128
	v_mul_f32_e32 v37, v37, v127
	v_mul_f32_e32 v32, v32, v124
	v_mul_f32_e32 v33, v33, v123
	v_mul_f32_e32 v29, v96, v29
	v_mul_f32_e32 v30, v96, v30
	v_mul_f32_e32 v31, v96, v31
	v_mul_f32_e32 v24, v96, v24
	v_mul_f32_e32 v26, v96, v26
	v_mul_f32_e32 v27, v96, v27
	v_med3_f32 v6, v6, s70, v178
	v_med3_f32 v7, v7, s70, v178
	global_load_lds_dwordx4 v154, s[38:39]
	v_add_u32_e32 v185, 0, v4
	v_mul_f32_e32 v29, v29, v135
	v_mul_f32_e32 v30, v30, v134
	v_mul_f32_e32 v31, v31, v133
	v_mul_f32_e32 v24, v24, v132
	v_mul_f32_e32 v26, v26, v130
	v_mul_f32_e32 v27, v27, v129
	v_med3_f32 v60, v60, s70, v178
	v_med3_f32 v61, v61, s70, v178
	v_mov_b32_e32 v128, v153
	v_med3_f32 v56, v56, s70, v178
	v_med3_f32 v57, v57, s70, v178
	v_mov_b32_e32 v129, v153
	v_med3_f32 v52, v52, s70, v178
	v_med3_f32 v53, v53, s70, v178
	v_mov_b32_e32 v130, v153
	v_med3_f32 v44, v44, s70, v178
	v_med3_f32 v45, v45, s70, v178
	v_mov_b32_e32 v132, v153
	v_med3_f32 v40, v40, s70, v178
	v_med3_f32 v41, v41, s70, v178
	v_mov_b32_e32 v133, v153
	v_med3_f32 v36, v36, s70, v178
	v_med3_f32 v37, v37, s70, v178
	v_mov_b32_e32 v134, v153
	v_med3_f32 v32, v32, s70, v178
	v_med3_f32 v33, v33, s70, v178
	v_mov_b32_e32 v135, v153
	v_cvt_pk_fp8_f32 v142, v6, v7 op_sel:[0,0,1]
	s_waitcnt vmcnt(0)
	s_waitcnt vmcnt(0) lgkmcnt(0)
	s_barrier
	ds_read_b128 v[0:3], v184 offset:32768
	ds_read_b128 v[4:7], v185 offset:32768
	v_mul_f32_e32 v12, v96, v12
	v_mul_f32_e32 v13, v96, v13
	v_cvt_pk_fp8_f32 v128, v60, v61
	v_cvt_pk_fp8_f32 v129, v56, v57
	v_cvt_pk_fp8_f32 v130, v52, v53
	v_cvt_pk_fp8_f32 v132, v44, v45
	v_cvt_pk_fp8_f32 v133, v40, v41
	v_cvt_pk_fp8_f32 v134, v36, v37
	v_cvt_pk_fp8_f32 v135, v32, v33
	v_mul_f32_e32 v62, v62, v96
	v_mul_f32_e32 v63, v63, v96
	v_mul_f32_e32 v58, v58, v96
	v_mul_f32_e32 v59, v59, v96
	v_mul_f32_e32 v54, v54, v96
	v_mul_f32_e32 v55, v55, v96
	v_mul_f32_e32 v46, v96, v46
	v_mul_f32_e32 v47, v96, v47
	v_mul_f32_e32 v42, v96, v42
	v_mul_f32_e32 v43, v96, v43
	v_mul_f32_e32 v38, v96, v38
	v_mul_f32_e32 v39, v96, v39
	v_mul_f32_e32 v34, v96, v34
	v_mul_f32_e32 v35, v96, v35
	v_mul_f32_e32 v16, v96, v16
	v_mul_f32_e32 v12, v12, v151
	v_mul_f32_e32 v13, v13, v150
	v_mul_f32_e32 v62, v62, v102
	v_mul_f32_e32 v63, v63, v101
	v_mul_f32_e32 v58, v58, v98
	v_mul_f32_e32 v59, v59, v97
	v_mul_f32_e32 v54, v54, v110
	v_mul_f32_e32 v55, v55, v109
	v_mul_f32_e32 v46, v46, v118
	v_mul_f32_e32 v47, v47, v117
	v_mul_f32_e32 v42, v42, v114
	v_mul_f32_e32 v43, v43, v113
	v_mul_f32_e32 v38, v38, v126
	v_mul_f32_e32 v39, v39, v125
	v_mul_f32_e32 v34, v34, v122
	v_mul_f32_e32 v35, v35, v121
	v_mul_f32_e32 v16, v16, v140
	v_med3_f32 v12, v12, s70, v178
	v_med3_f32 v13, v13, s70, v178
	v_mov_b32_e32 v140, v153
	v_med3_f32 v62, v62, s70, v178
	v_med3_f32 v63, v63, s70, v178
	v_med3_f32 v56, v58, s70, v178
	v_med3_f32 v57, v59, s70, v178
	v_med3_f32 v54, v54, s70, v178
	v_med3_f32 v55, v55, s70, v178
	v_med3_f32 v46, v46, s70, v178
	v_med3_f32 v47, v47, s70, v178
	v_med3_f32 v40, v42, s70, v178
	v_med3_f32 v41, v43, s70, v178
	v_med3_f32 v38, v38, s70, v178
	v_med3_f32 v39, v39, s70, v178
	v_med3_f32 v32, v34, s70, v178
	v_med3_f32 v33, v35, s70, v178
	v_cvt_pk_fp8_f32 v140, v12, v13
	v_or_b32_e32 v50, 0x2000, v49
	v_mul_f32_e32 v17, v96, v17
	v_mul_f32_e32 v14, v96, v14
	v_mul_f32_e32 v15, v96, v15
	v_cvt_pk_fp8_f32 v128, v62, v63 op_sel:[0,0,1]
	v_cvt_pk_fp8_f32 v129, v56, v57 op_sel:[0,0,1]
	v_cvt_pk_fp8_f32 v130, v54, v55 op_sel:[0,0,1]
	v_cvt_pk_fp8_f32 v132, v46, v47 op_sel:[0,0,1]
	v_cvt_pk_fp8_f32 v133, v40, v41 op_sel:[0,0,1]
	v_cvt_pk_fp8_f32 v134, v38, v39 op_sel:[0,0,1]
	v_cvt_pk_fp8_f32 v135, v32, v33 op_sel:[0,0,1]
	v_add_u32_e32 v12, v8, v50
	v_mul_f32_e32 v17, v17, v139
	v_mul_f32_e32 v14, v14, v149
	v_mul_f32_e32 v15, v15, v148
	v_xor_b32_e32 v12, 16, v12
	v_med3_f32 v16, v16, s70, v178
	v_med3_f32 v17, v17, s70, v178
	v_mov_b32_e32 v139, v153
	v_med3_f32 v14, v14, s70, v178
	v_med3_f32 v15, v15, s70, v178
	v_add_u32_e32 v186, 0, v12
	v_cvt_pk_fp8_f32 v139, v16, v17
	v_cvt_pk_fp8_f32 v140, v14, v15 op_sel:[0,0,1]
	ds_read_b128 v[8:11], v184 offset:40960
	ds_read_b128 v[12:15], v186 offset:32768
	v_mul_f32_e32 v18, v96, v18
	v_mul_f32_e32 v19, v96, v19
	s_waitcnt lgkmcnt(2)
	v_mfma_f32_32x32x64_f8f6f4 v[32:47], v[0:7], v[128:135], 0
	v_med3_f32 v0, v74, s70, v178
	v_med3_f32 v1, v75, s70, v178
	v_mov_b32_e32 v149, v153
	v_mul_f32_e32 v28, v96, v28
	v_mul_f32_e32 v18, v18, v138
	v_mul_f32_e32 v19, v19, v137
	v_cvt_pk_fp8_f32 v149, v0, v1
	v_mul_f32_e32 v28, v28, v136
	v_med3_f32 v16, v18, s70, v178
	v_med3_f32 v17, v19, s70, v178
	v_med3_f32 v28, v28, s70, v178
	v_med3_f32 v29, v29, s70, v178
	v_mov_b32_e32 v136, v153
	v_med3_f32 v24, v24, s70, v178
	v_med3_f32 v25, v25, s70, v178
	v_mov_b32_e32 v137, v153
	v_med3_f32 v20, v20, s70, v178
	v_med3_f32 v21, v21, s70, v178
	v_mov_b32_e32 v138, v153
	v_cvt_pk_fp8_f32 v139, v16, v17 op_sel:[0,0,1]
	v_med3_f32 v16, v78, s70, v178
	v_med3_f32 v17, v79, s70, v178
	v_mov_b32_e32 v148, v153
	v_cvt_pk_fp8_f32 v136, v28, v29
	v_cvt_pk_fp8_f32 v137, v24, v25
	v_cvt_pk_fp8_f32 v138, v20, v21
	v_cvt_pk_fp8_f32 v148, v16, v17
	v_med3_f32 v0, v70, s70, v178
	v_med3_f32 v1, v71, s70, v178
	v_cvt_pk_fp8_f32 v149, v0, v1 op_sel:[0,0,1]
	v_med3_f32 v0, v68, s70, v178
	v_med3_f32 v1, v69, s70, v178
	v_mov_b32_e32 v150, v153
	v_cvt_pk_fp8_f32 v150, v0, v1
	v_add_u32_e32 v0, 4, v48
	v_med3_f32 v30, v30, s70, v178
	v_med3_f32 v31, v31, s70, v178
	v_med3_f32 v24, v26, s70, v178
	v_med3_f32 v25, v27, s70, v178
	v_med3_f32 v22, v22, s70, v178
	v_med3_f32 v23, v23, s70, v178
	v_med3_f32 v18, v76, s70, v178
	v_med3_f32 v19, v77, s70, v178
	v_bitop3_b32 v0, v0, v180, 15 bitop3:0x78
	v_cvt_pk_fp8_f32 v136, v30, v31 op_sel:[0,0,1]
	v_cvt_pk_fp8_f32 v137, v24, v25 op_sel:[0,0,1]
	v_cvt_pk_fp8_f32 v138, v22, v23 op_sel:[0,0,1]
	v_cvt_pk_fp8_f32 v148, v18, v19 op_sel:[0,0,1]
	s_waitcnt lgkmcnt(0)
	v_mfma_f32_32x32x64_f8f6f4 v[16:31], v[8:15], v[128:135], 0
	v_lshlrev_b32_e32 v8, 4, v0
	v_add_u32_e32 v4, v8, v49
	v_add_u32_e32 v187, 0, v4
	v_xor_b32_e32 v4, 16, v4
	v_add_u32_e32 v188, 0, v4
	ds_read_b128 v[0:3], v187 offset:32768
	ds_read_b128 v[4:7], v188 offset:32768
	v_add_u32_e32 v12, v8, v50
	v_xor_b32_e32 v12, 16, v12
	v_add_u32_e32 v189, 0, v12
	v_med3_f32 v53, v66, s70, v178
	v_med3_f32 v54, v67, s70, v178
	v_mov_b32_e32 v151, v153
	ds_read_b128 v[8:11], v187 offset:40960
	ds_read_b128 v[12:15], v189 offset:32768
	v_cvt_pk_fp8_f32 v151, v53, v54
	s_waitcnt lgkmcnt(2)
	v_mfma_f32_32x32x64_f8f6f4 v[32:47], v[0:7], v[136:143], v[32:47]
	v_med3_f32 v0, v64, s70, v178
	v_med3_f32 v1, v65, s70, v178
	v_cvt_pk_fp8_f32 v151, v0, v1 op_sel:[0,0,1]
	v_lshlrev_b32_e32 v0, 3, v180
	v_and_b32_e32 v1, 0xc0, v182
	v_lshlrev_b32_e32 v2, 1, v180
	v_and_or_b32 v1, v0, 24, v1
	v_and_b32_e32 v2, 32, v2
	v_and_b32_e32 v0, 0x100, v0
	v_or3_b32 v56, v1, v2, v0
	v_add_u32_e32 v0, 8, v48
	v_bitop3_b32 v0, v0, v180, 15 bitop3:0x78
	v_med3_f32 v51, v72, s70, v178
	v_med3_f32 v52, v73, s70, v178
	v_cvt_pk_fp8_f32 v150, v51, v52 op_sel:[0,0,1]
	s_waitcnt lgkmcnt(0)
	v_mfma_f32_32x32x64_f8f6f4 v[16:31], v[8:15], v[136:143], v[16:31]
	v_lshlrev_b32_e32 v8, 4, v0
	v_add_u32_e32 v4, v8, v49
	v_add_u32_e32 v191, 0, v4
	v_xor_b32_e32 v4, 16, v4
	v_add_u32_e32 v192, 0, v4
	ds_read_b128 v[0:3], v191 offset:32768
	ds_read_b128 v[4:7], v192 offset:32768
	v_add_u32_e32 v8, v8, v50
	v_xor_b32_e32 v8, 16, v8
	s_mov_b32 s36, s37
	v_add_u32_e32 v193, 0, v8
	ds_read_b128 v[48:51], v191 offset:40960
	ds_read_b128 v[52:55], v193 offset:32768
	s_mov_b32 s38, s37
	s_mov_b32 s39, s37
	s_waitcnt lgkmcnt(2)
	v_mfma_f32_32x32x64_f8f6f4 v[32:47], v[0:7], v[144:151], v[32:47]
	s_mov_b32 s40, s37
	s_mov_b32 s41, s37
	s_mov_b32 s42, s37
	s_mov_b32 s43, s37
	s_mov_b32 s44, s37
	s_mov_b32 s45, s37
	s_mov_b32 s46, s37
	s_mov_b32 s47, s37
	s_mov_b32 s48, s37
	s_mov_b32 s49, s37
	s_mov_b32 s50, s37
	s_mov_b32 s51, s37
	v_mov_b64_e32 v[0:1], s[36:37]
	v_mov_b64_e32 v[2:3], s[38:39]
	v_mov_b64_e32 v[4:5], s[40:41]
	v_mov_b64_e32 v[6:7], s[42:43]
	v_mov_b64_e32 v[8:9], s[44:45]
	v_mov_b64_e32 v[10:11], s[46:47]
	v_mov_b64_e32 v[12:13], s[48:49]
	v_mov_b64_e32 v[14:15], s[50:51]
	s_add_u32 s38, s64, 0x60000
	s_addc_u32 s39, s65, 0
	s_mov_b32 m0, s57
	s_add_u32 s4, s4, 0x58280100
	s_waitcnt lgkmcnt(0)
	s_waitcnt lgkmcnt(0)
	s_barrier
	global_load_lds_dwordx4 v152, s[38:39]
	s_mov_b32 m0, s86
	s_addc_u32 s5, s5, 0
	s_add_i32 s40, s56, 0x4000
	global_load_lds_dwordx4 v154, s[38:39]
	s_mov_b32 m0, s40
	s_add_i32 s41, s56, 0x6000
	global_load_lds_dwordx4 v156, s[4:5]
	s_mov_b32 m0, s41
	v_mfma_f32_32x32x64_f8f6f4 v[16:31], v[48:55], v[144:151], v[16:31]
	global_load_lds_dwordx4 v158, s[4:5]
	v_max_f32_e32 v48, v33, v33
	v_max_f32_e32 v49, v32, v32
	v_max_f32_e32 v48, v49, v48
	v_max3_f32 v48, v48, v34, v35
	v_max3_f32 v48, v48, v36, v37
	v_max3_f32 v48, v48, v38, v39
	v_max3_f32 v48, v48, v40, v41
	v_max3_f32 v48, v48, v42, v43
	v_max3_f32 v48, v48, v44, v45
	v_max3_f32 v48, v48, v46, v47
	s_add_i32 s42, s33, -1
	v_add_u32_e32 v190, s6, v56
	s_mov_b32 s19, 4
	s_nop 5
	v_max3_f32 v48, v48, v16, v17
	v_max3_f32 v48, v48, v18, v19
	v_max3_f32 v48, v48, v20, v21
	v_max3_f32 v48, v48, v22, v23
	v_max3_f32 v48, v48, v24, v25
	v_max3_f32 v48, v48, v26, v27
	v_max3_f32 v48, v48, v28, v29
	v_max3_f32 v48, v48, v30, v31
	v_mov_b32_e32 v49, v48
	s_nop 1
	v_permlane32_swap_b32_e32 v48, v49
	v_max_f32_e32 v49, v49, v49
	v_max_f32_e32 v48, v48, v48
	v_max_f32_e32 v48, v48, v49
	v_add_f32_e32 v49, 0x7149f2ca, v48
	v_cmp_ge_f32_e32 vcc, s93, v49
	s_cmp_eq_u64 vcc, exec
	v_max_f32_e32 v49, 0xf149f2ca, v48
	s_cselect_b64 vcc, -1, 0
	v_cndmask_b32_e32 v195, v49, v179, vcc
	v_mul_f32_e32 v48, 0xbdd53b94, v195
	v_fmamk_f32 v32, v32, 0x3dd53b94, v48
	v_exp_f32_e32 v64, v32
	v_fmamk_f32 v32, v33, 0x3dd53b94, v48
	v_exp_f32_e32 v65, v32
	v_fmamk_f32 v32, v34, 0x3dd53b94, v48
	v_exp_f32_e32 v66, v32
	v_fmamk_f32 v32, v35, 0x3dd53b94, v48
	v_exp_f32_e32 v67, v32
	v_fmamk_f32 v32, v36, 0x3dd53b94, v48
	v_exp_f32_e32 v68, v32
	v_fmamk_f32 v32, v37, 0x3dd53b94, v48
	v_exp_f32_e32 v69, v32
	v_fmamk_f32 v32, v38, 0x3dd53b94, v48
	v_exp_f32_e32 v70, v32
	v_fmamk_f32 v32, v39, 0x3dd53b94, v48
	v_exp_f32_e32 v71, v32
	v_fmamk_f32 v32, v40, 0x3dd53b94, v48
	v_exp_f32_e32 v72, v32
	v_fmamk_f32 v32, v41, 0x3dd53b94, v48
	v_exp_f32_e32 v73, v32
	v_fmamk_f32 v32, v42, 0x3dd53b94, v48
	v_exp_f32_e32 v74, v32
	v_fmamk_f32 v32, v43, 0x3dd53b94, v48
	v_exp_f32_e32 v75, v32
	v_fmamk_f32 v32, v44, 0x3dd53b94, v48
	v_pk_fma_f32 v[86:87], v[22:23], s[54:55], v[48:49] op_sel_hi:[1,0,0]
	v_sub_f32_e32 v22, 0xf149f2ca, v49
	v_exp_f32_e32 v76, v32
	v_fmamk_f32 v32, v45, 0x3dd53b94, v48
	v_mul_f32_e32 v22, 0x3dd53b94, v22
	v_exp_f32_e32 v77, v32
	v_fmamk_f32 v32, v46, 0x3dd53b94, v48
	v_exp_f32_e32 v22, v22
	v_exp_f32_e32 v78, v32
	v_fmamk_f32 v32, v47, 0x3dd53b94, v48
	v_exp_f32_e32 v79, v32
	s_addk_i32 s6, 0x4000
	v_pk_fma_f32 v[94:95], v[30:31], s[54:55], v[48:49] op_sel_hi:[1,0,0]
	v_pk_fma_f32 v[92:93], v[28:29], s[54:55], v[48:49] op_sel_hi:[1,0,0]
	v_pk_fma_f32 v[90:91], v[26:27], s[54:55], v[48:49] op_sel_hi:[1,0,0]
	v_pk_fma_f32 v[88:89], v[24:25], s[54:55], v[48:49] op_sel_hi:[1,0,0]
	v_pk_fma_f32 v[84:85], v[20:21], s[54:55], v[48:49] op_sel_hi:[1,0,0]
	v_pk_fma_f32 v[82:83], v[18:19], s[54:55], v[48:49] op_sel_hi:[1,0,0]
	v_pk_fma_f32 v[80:81], v[16:17], s[54:55], v[48:49] op_sel_hi:[1,0,0]
	v_cndmask_b32_e64 v201, v22, 1.0, vcc
	v_add_u32_e32 v199, s6, v56
	v_mov_b64_e32 v[62:63], v[14:15]
	v_mov_b64_e32 v[46:47], v[14:15]
	v_mov_b64_e32 v[30:31], v[14:15]
	v_mov_b32_e32 v155, v153
	v_mov_b32_e32 v157, v153
	v_mov_b32_e32 v159, v153
	v_cmp_gt_u32_e64 s[4:5], 32, v180
	v_lshl_add_u32 v197, v181, 2, s77
	v_lshlrev_b32_e32 v196, 4, v183
	v_mov_b32_e32 v198, 0
	v_mov_b64_e32 v[60:61], v[12:13]
	v_mov_b64_e32 v[58:59], v[10:11]
	v_mov_b64_e32 v[56:57], v[8:9]
	v_mov_b64_e32 v[54:55], v[6:7]
	v_mov_b64_e32 v[52:53], v[4:5]
	v_mov_b64_e32 v[50:51], v[2:3]
	v_mov_b64_e32 v[48:49], v[0:1]
	v_mov_b64_e32 v[44:45], v[12:13]
	v_mov_b64_e32 v[42:43], v[10:11]
	v_mov_b64_e32 v[40:41], v[8:9]
	v_mov_b64_e32 v[38:39], v[6:7]
	v_mov_b64_e32 v[36:37], v[4:5]
	v_mov_b64_e32 v[34:35], v[2:3]
	v_mov_b64_e32 v[32:33], v[0:1]
	v_mov_b64_e32 v[28:29], v[12:13]
	v_mov_b64_e32 v[26:27], v[10:11]
	v_mov_b64_e32 v[24:25], v[8:9]
	v_mov_b64_e32 v[22:23], v[6:7]
	v_mov_b64_e32 v[20:21], v[4:5]
	v_mov_b64_e32 v[18:19], v[2:3]
	v_mov_b64_e32 v[16:17], v[0:1]
.LBB0_503:
	s_add_i32 s36, s19, -3
	s_cmp_lt_u32 s36, s33
	s_cselect_b64 s[6:7], -1, 0
	s_cmp_ge_u32 s36, s33
	ds_read_b128 v[100:103], v185 offset:49152
	ds_read_b128 v[96:99], v184 offset:49152
	ds_read_b128 v[104:107], v184 offset:57344
	ds_read_b128 v[108:111], v186 offset:49152
	ds_read_b128 v[224:227], v188 offset:49152
	ds_read_b128 v[220:223], v187 offset:49152
	ds_read_b128 v[228:231], v187 offset:57344
	ds_read_b128 v[232:235], v189 offset:49152
	v_add_f32_e32 v202, 0, v64
	v_add_f32_e32 v202, v65, v202
	v_add_f32_e32 v202, v66, v202
	v_add_f32_e32 v202, v67, v202
	v_add_f32_e32 v202, v68, v202
	v_add_f32_e32 v202, v69, v202
	v_add_f32_e32 v202, v70, v202
	v_add_f32_e32 v202, v71, v202
	v_add_f32_e32 v202, v72, v202
	v_add_f32_e32 v202, v73, v202
	s_waitcnt lgkmcnt(0)
	v_mfma_f32_32x32x64_f8f6f4 v[112:127], v[96:103], v[128:135], 0
	v_add_f32_e32 v202, v74, v202
	v_add_f32_e32 v202, v75, v202
	v_exp_f32_e32 v80, v80
	v_add_f32_e32 v202, v76, v202
	v_exp_f32_e32 v81, v81
	v_add_f32_e32 v202, v77, v202
	v_exp_f32_e32 v82, v82
	v_add_f32_e32 v202, v78, v202
	v_mfma_f32_32x32x64_f8f6f4 v[96:111], v[104:111], v[128:135], 0
	v_exp_f32_e32 v83, v83
	v_add_f32_e32 v202, v79, v202
	v_exp_f32_e32 v84, v84
	v_add_f32_e32 v202, v80, v202
	v_exp_f32_e32 v85, v85
	v_add_f32_e32 v202, v81, v202
	v_exp_f32_e32 v86, v86
	v_add_f32_e32 v202, v82, v202
	v_mfma_f32_32x32x64_f8f6f4 v[112:127], v[220:227], v[136:143], v[112:127]
	v_exp_f32_e32 v87, v87
	v_add_f32_e32 v202, v83, v202
	v_exp_f32_e32 v88, v88
	v_add_f32_e32 v202, v84, v202
	v_exp_f32_e32 v89, v89
	v_add_f32_e32 v202, v85, v202
	v_exp_f32_e32 v90, v90
	v_add_f32_e32 v202, v86, v202
	v_mfma_f32_32x32x64_f8f6f4 v[96:111], v[228:235], v[136:143], v[96:111]
	v_exp_f32_e32 v91, v91
	v_add_f32_e32 v202, v87, v202
	v_exp_f32_e32 v92, v92
	v_add_f32_e32 v202, v88, v202
	v_exp_f32_e32 v93, v93
	v_add_f32_e32 v202, v89, v202
	v_exp_f32_e32 v94, v94
	v_add_f32_e32 v202, v90, v202
	ds_read_b128 v[224:227], v192 offset:49152
	ds_read_b128 v[220:223], v191 offset:49152
	ds_read_b128 v[228:231], v191 offset:57344
	ds_read_b128 v[232:235], v193 offset:49152
	v_exp_f32_e32 v95, v95
	v_add_f32_e32 v202, v91, v202
	v_add_f32_e32 v202, v92, v202
	v_add_f32_e32 v202, v93, v202
	v_add_f32_e32 v202, v94, v202
	v_add_f32_e32 v202, v95, v202
	v_mov_b32_e32 v203, v202
	s_nop 1
	s_waitcnt lgkmcnt(0)
	v_mfma_f32_32x32x64_f8f6f4 v[112:127], v[220:227], v[144:151], v[112:127]
	v_permlane32_swap_b32_e32 v202, v203
	v_cvt_pk_bf16_f32 v204, v64, v65
	v_cvt_pk_bf16_f32 v205, v66, v67
	v_cvt_pk_bf16_f32 v206, v68, v69
	v_cvt_pk_bf16_f32 v207, v70, v71
	v_cvt_pk_bf16_f32 v208, v72, v73
	v_cvt_pk_bf16_f32 v209, v74, v75
	v_cvt_pk_bf16_f32 v210, v76, v77
	v_cvt_pk_bf16_f32 v211, v78, v79
	v_cvt_pk_bf16_f32 v212, v80, v81
	v_cvt_pk_bf16_f32 v213, v82, v83
	v_mfma_f32_32x32x64_f8f6f4 v[96:111], v[228:235], v[144:151], v[96:111]
	v_cvt_pk_bf16_f32 v214, v84, v85
	v_cvt_pk_bf16_f32 v215, v86, v87
	v_cvt_pk_bf16_f32 v216, v88, v89
	v_cvt_pk_bf16_f32 v217, v90, v91
	v_cvt_pk_bf16_f32 v218, v92, v93
	v_cvt_pk_bf16_f32 v219, v94, v95
	s_nop 0
	ds_read_b64_tr_b16 v[220:221], v190 offset:0
	ds_read_b64_tr_b16 v[222:223], v190 offset:0x800
	ds_read_b64_tr_b16 v[224:225], v190 offset:0x1000
	ds_read_b64_tr_b16 v[226:227], v190 offset:0x1800
	ds_read_b64_tr_b16 v[228:229], v190 offset:0x2000
	ds_read_b64_tr_b16 v[230:231], v190 offset:0x2800
	ds_read_b64_tr_b16 v[232:233], v190 offset:0x3000
	ds_read_b64_tr_b16 v[234:235], v190 offset:0x3800
	v_max_f32_e32 v200, v113, v113
	v_max_f32_e32 v240, v112, v112
	v_max_f32_e32 v200, v240, v200
	v_max3_f32 v200, v200, v114, v115
	v_max3_f32 v200, v200, v116, v117
	v_max3_f32 v200, v200, v118, v119
	v_max3_f32 v200, v200, v120, v121
	v_max3_f32 v200, v200, v122, v123
	s_waitcnt lgkmcnt(0)
	s_nop 0
	v_mfma_f32_32x32x16_bf16 v[0:15], v[204:207], v[220:223], v[0:15]
	v_max3_f32 v200, v200, v124, v125
	v_max3_f32 v200, v200, v126, v127
	v_max3_f32 v200, v200, v96, v97
	v_max3_f32 v200, v200, v98, v99
	v_max3_f32 v200, v200, v100, v101
	ds_read_b64_tr_b16 v[220:221], v190 offset:0x200
	ds_read_b64_tr_b16 v[222:223], v190 offset:0xa00
	v_mfma_f32_32x32x16_bf16 v[0:15], v[208:211], v[224:227], v[0:15]
	v_max3_f32 v200, v200, v102, v103
	v_max3_f32 v200, v200, v104, v105
	v_max3_f32 v200, v200, v106, v107
	v_max3_f32 v200, v200, v108, v109
	v_max3_f32 v200, v200, v110, v111
	ds_read_b64_tr_b16 v[224:225], v190 offset:0x1200
	ds_read_b64_tr_b16 v[226:227], v190 offset:0x1a00
	v_mfma_f32_32x32x16_bf16 v[0:15], v[212:215], v[228:231], v[0:15]
	v_mov_b32_e32 v240, v200
	s_nop 1
	v_permlane32_swap_b32_e32 v200, v240
	ds_read_b64_tr_b16 v[228:229], v190 offset:0x2200
	ds_read_b64_tr_b16 v[230:231], v190 offset:0x2a00
	ds_read_b64_tr_b16 v[236:237], v190 offset:0x3200
	ds_read_b64_tr_b16 v[238:239], v190 offset:0x3a00
	v_max_f32_e32 v240, v240, v240
	v_max_f32_e32 v200, v200, v200
	v_max_f32_e32 v200, v200, v240
	v_sub_f32_e32 v240, v200, v195
	v_cmp_ge_f32_e32 vcc, s93, v240
	v_max_f32_e32 v240, v195, v195
	v_max_f32_e32 v240, v240, v200
	v_sub_f32_e32 v200, v195, v240
	s_waitcnt lgkmcnt(0)
	v_mfma_f32_32x32x16_bf16 v[0:15], v[216:219], v[232:235], v[0:15]
	v_mul_f32_e32 v200, 0x3dd53b94, v200
	v_exp_f32_e32 v200, v200
	s_cmp_eq_u64 vcc, exec
	s_cselect_b64 s[6:7], -1, 0
	v_mfma_f32_32x32x16_bf16 v[48:63], v[204:207], v[220:223], v[48:63]
	v_cndmask_b32_e64 v200, v200, 1.0, s[6:7]
	v_cmp_gt_f32_e32 vcc, 1.0, v200
	v_cndmask_b32_e64 v195, v240, v195, s[6:7]
	v_mul_f32_e32 v240, 0xbdd53b94, v195
	v_mov_b32_e32 v241, v240
	ds_read_b64_tr_b16 v[220:221], v190 offset:0x400
	ds_read_b64_tr_b16 v[222:223], v190 offset:0xc00
	v_mfma_f32_32x32x16_bf16 v[48:63], v[208:211], v[224:227], v[48:63]
	v_fmamk_f32 v112, v112, 0x3dd53b94, v240
	v_fmamk_f32 v113, v113, 0x3dd53b94, v240
	v_fmamk_f32 v114, v114, 0x3dd53b94, v240
	v_fmamk_f32 v115, v115, 0x3dd53b94, v240
	v_fmamk_f32 v116, v116, 0x3dd53b94, v240
	ds_read_b64_tr_b16 v[224:225], v190 offset:0x1400
	ds_read_b64_tr_b16 v[226:227], v190 offset:0x1c00
	v_mfma_f32_32x32x16_bf16 v[48:63], v[212:215], v[228:231], v[48:63]
	v_fmamk_f32 v117, v117, 0x3dd53b94, v240
	v_fmamk_f32 v118, v118, 0x3dd53b94, v240
	v_fmamk_f32 v119, v119, 0x3dd53b94, v240
	v_fmamk_f32 v120, v120, 0x3dd53b94, v240
	v_fmamk_f32 v121, v121, 0x3dd53b94, v240
	ds_read_b64_tr_b16 v[228:229], v190 offset:0x2400
	ds_read_b64_tr_b16 v[230:231], v190 offset:0x2c00
	ds_read_b64_tr_b16 v[232:233], v190 offset:0x3400
	ds_read_b64_tr_b16 v[234:235], v190 offset:0x3c00
	v_fmamk_f32 v122, v122, 0x3dd53b94, v240
	v_fmamk_f32 v123, v123, 0x3dd53b94, v240
	v_fmamk_f32 v124, v124, 0x3dd53b94, v240
	v_fmamk_f32 v125, v125, 0x3dd53b94, v240
	v_fmamk_f32 v126, v126, 0x3dd53b94, v240
	v_fmac_f32_e32 v241, 0x3dd53b94, v127
	v_exp_f32_e32 v112, v112
	s_waitcnt lgkmcnt(0)
	v_mfma_f32_32x32x16_bf16 v[48:63], v[216:219], v[236:239], v[48:63]
	v_exp_f32_e32 v113, v113
	v_exp_f32_e32 v114, v114
	v_mfma_f32_32x32x16_bf16 v[32:47], v[204:207], v[220:223], v[32:47]
	v_exp_f32_e32 v115, v115
	v_exp_f32_e32 v116, v116
	ds_read_b64_tr_b16 v[220:221], v190 offset:0x600
	ds_read_b64_tr_b16 v[222:223], v190 offset:0xe00
	v_mfma_f32_32x32x16_bf16 v[32:47], v[208:211], v[224:227], v[32:47]
	v_exp_f32_e32 v117, v117
	v_exp_f32_e32 v118, v118
	ds_read_b64_tr_b16 v[224:225], v190 offset:0x1600
	ds_read_b64_tr_b16 v[226:227], v190 offset:0x1e00
	v_mfma_f32_32x32x16_bf16 v[32:47], v[212:215], v[228:231], v[32:47]
	v_exp_f32_e32 v119, v119
	v_exp_f32_e32 v120, v120
	ds_read_b64_tr_b16 v[228:229], v190 offset:0x2600
	ds_read_b64_tr_b16 v[230:231], v190 offset:0x2e00
	ds_read_b64_tr_b16 v[236:237], v190 offset:0x3600
	ds_read_b64_tr_b16 v[238:239], v190 offset:0x3e00
	v_exp_f32_e32 v121, v121
	v_exp_f32_e32 v122, v122
	v_exp_f32_e32 v123, v123
	v_exp_f32_e32 v124, v124
	s_waitcnt lgkmcnt(0)
	v_mfma_f32_32x32x16_bf16 v[32:47], v[216:219], v[232:235], v[32:47]
	v_exp_f32_e32 v125, v125
	v_exp_f32_e32 v126, v126
	v_mfma_f32_32x32x16_bf16 v[16:31], v[204:207], v[220:223], v[16:31]
	v_exp_f32_e32 v127, v241
	v_pk_fma_f32 v[110:111], v[110:111], s[54:55], v[240:241] op_sel_hi:[1,0,0]
	v_mfma_f32_32x32x16_bf16 v[16:31], v[208:211], v[224:227], v[16:31]
	v_pk_fma_f32 v[108:109], v[108:109], s[54:55], v[240:241] op_sel_hi:[1,0,0]
	v_pk_fma_f32 v[106:107], v[106:107], s[54:55], v[240:241] op_sel_hi:[1,0,0]
	v_mfma_f32_32x32x16_bf16 v[16:31], v[212:215], v[228:231], v[16:31]
	v_pk_fma_f32 v[104:105], v[104:105], s[54:55], v[240:241] op_sel_hi:[1,0,0]
	v_pk_fma_f32 v[102:103], v[102:103], s[54:55], v[240:241] op_sel_hi:[1,0,0]
	v_mfma_f32_32x32x16_bf16 v[16:31], v[216:219], v[236:239], v[16:31]
	v_pk_fma_f32 v[100:101], v[100:101], s[54:55], v[240:241] op_sel_hi:[1,0,0]
	v_pk_fma_f32 v[98:99], v[98:99], s[54:55], v[240:241] op_sel_hi:[1,0,0]
	v_pk_fma_f32 v[96:97], v[96:97], s[54:55], v[240:241] op_sel_hi:[1,0,0]
	s_cbranch_vccz .Latt0_nrA
	s_nop 7
	s_nop 7
	s_and_saveexec_b64 s[38:39], s[4:5]
	ds_write_b32 v197, v200 offset:128
	s_or_b64 exec, exec, s[38:39]
	s_waitcnt lgkmcnt(0)
	v_add_u32_e32 v205, s77, v196
	ds_read_b128 v[206:209], v205 offset:224
	ds_read_b128 v[210:213], v205 offset:192
	ds_read_b128 v[214:217], v205 offset:160
	ds_read_b128 v[218:221], v205 offset:128
	s_waitcnt lgkmcnt(0)
	v_pk_mul_f32 v[12:13], v[12:13], v[206:207]
	v_pk_mul_f32 v[8:9], v[8:9], v[210:211]
	v_pk_mul_f32 v[4:5], v[4:5], v[214:215]
	v_pk_mul_f32 v[14:15], v[14:15], v[208:209]
	v_pk_mul_f32 v[10:11], v[10:11], v[212:213]
	v_pk_mul_f32 v[6:7], v[6:7], v[216:217]
	v_pk_mul_f32 v[2:3], v[2:3], v[220:221]
	v_pk_mul_f32 v[0:1], v[0:1], v[218:219]
	v_pk_mul_f32 v[60:61], v[60:61], v[206:207]
	v_pk_mul_f32 v[56:57], v[56:57], v[210:211]
	v_pk_mul_f32 v[52:53], v[52:53], v[214:215]
	v_pk_mul_f32 v[62:63], v[62:63], v[208:209]
	v_pk_mul_f32 v[58:59], v[58:59], v[212:213]
	v_pk_mul_f32 v[54:55], v[54:55], v[216:217]
	v_pk_mul_f32 v[50:51], v[50:51], v[220:221]
	v_pk_mul_f32 v[48:49], v[48:49], v[218:219]
	v_pk_mul_f32 v[44:45], v[44:45], v[206:207]
	v_pk_mul_f32 v[40:41], v[40:41], v[210:211]
	v_pk_mul_f32 v[36:37], v[36:37], v[214:215]
	v_pk_mul_f32 v[46:47], v[46:47], v[208:209]
	v_pk_mul_f32 v[42:43], v[42:43], v[212:213]
	v_pk_mul_f32 v[38:39], v[38:39], v[216:217]
	v_pk_mul_f32 v[34:35], v[34:35], v[220:221]
	v_pk_mul_f32 v[32:33], v[32:33], v[218:219]
	v_pk_mul_f32 v[28:29], v[28:29], v[206:207]
	v_pk_mul_f32 v[24:25], v[24:25], v[210:211]
	v_pk_mul_f32 v[20:21], v[20:21], v[214:215]
	v_pk_mul_f32 v[30:31], v[30:31], v[208:209]
	v_pk_mul_f32 v[26:27], v[26:27], v[212:213]
	v_pk_mul_f32 v[22:23], v[22:23], v[216:217]
	v_pk_mul_f32 v[18:19], v[18:19], v[220:221]
	v_pk_mul_f32 v[16:17], v[16:17], v[218:219]
.Latt0_nrA:
.LBB0_511:
	s_add_i32 s6, s19, -1
	s_min_u32 s36, s6, s42
	s_mul_i32 s6, s36, 0x30000
	s_add_u32 s6, s64, s6
	s_addc_u32 s7, s65, 0
	s_add_i32 s43, s19, -2
	s_mov_b32 m0, s95
	s_waitcnt vmcnt(0)
	v_lshl_add_u64 v[204:205], s[6:7], 0, v[152:153]
	s_cmp_lt_u32 s43, s33
	s_waitcnt lgkmcnt(0)
	s_waitcnt vmcnt(0) lgkmcnt(0)
	s_barrier
	global_load_lds_dwordx4 v[204:205], off
	v_lshl_add_u64 v[204:205], s[6:7], 0, v[154:155]
	s_cselect_b64 s[6:7], -1, 0
	s_min_u32 s38, s43, s42
	s_lshl_b32 s38, s38, 19
	s_add_u32 s38, s66, s38
	s_mov_b32 m0, s18
	s_addc_u32 s39, s67, 0
	global_load_lds_dwordx4 v[204:205], off
	v_lshl_add_u64 v[204:205], s[38:39], 0, v[156:157]
	s_mov_b32 m0, s56
	s_cmp_ge_u32 s43, s33
	global_load_lds_dwordx4 v[204:205], off
	v_lshl_add_u64 v[204:205], s[38:39], 0, v[158:159]
	s_mov_b32 m0, s91
	s_nop 0
	global_load_lds_dwordx4 v[204:205], off
	s_cbranch_scc1 .LBB0_513
	ds_read_b128 v[68:71], v185 offset:32768
	ds_read_b128 v[64:67], v184 offset:32768
	ds_read_b128 v[80:83], v184 offset:40960
	ds_read_b128 v[84:87], v186 offset:32768
	ds_read_b128 v[226:229], v188 offset:32768
	ds_read_b128 v[222:225], v187 offset:32768
	v_add_f32_e32 v204, 0, v112
	v_add_f32_e32 v204, v113, v204
	v_add_f32_e32 v204, v114, v204
	v_add_f32_e32 v204, v115, v204
	v_add_f32_e32 v204, v116, v204
	v_add_f32_e32 v204, v117, v204
	v_add_f32_e32 v204, v118, v204
	v_add_f32_e32 v204, v119, v204
	v_add_f32_e32 v204, v120, v204
	v_add_f32_e32 v204, v121, v204
	s_waitcnt lgkmcnt(0)
	v_mfma_f32_32x32x64_f8f6f4 v[64:79], v[64:71], v[128:135], 0
	v_add_f32_e32 v204, v122, v204
	v_add_f32_e32 v204, v123, v204
	v_exp_f32_e32 v96, v96
	v_add_f32_e32 v204, v124, v204
	v_exp_f32_e32 v97, v97
	v_add_f32_e32 v204, v125, v204
	v_exp_f32_e32 v98, v98
	v_add_f32_e32 v204, v126, v204
	v_mfma_f32_32x32x64_f8f6f4 v[80:95], v[80:87], v[128:135], 0
	v_exp_f32_e32 v99, v99
	v_add_f32_e32 v204, v127, v204
	v_exp_f32_e32 v100, v100
	v_add_f32_e32 v204, v96, v204
	v_exp_f32_e32 v101, v101
	v_add_f32_e32 v204, v97, v204
	v_exp_f32_e32 v102, v102
	v_add_f32_e32 v204, v98, v204
	v_mfma_f32_32x32x64_f8f6f4 v[64:79], v[222:229], v[136:143], v[64:79]
	v_exp_f32_e32 v103, v103
	v_add_f32_e32 v204, v99, v204
	v_exp_f32_e32 v104, v104
	v_add_f32_e32 v204, v100, v204
	v_exp_f32_e32 v105, v105
	v_add_f32_e32 v204, v101, v204
	v_exp_f32_e32 v106, v106
	v_add_f32_e32 v204, v102, v204
	ds_read_b128 v[222:225], v187 offset:40960
	ds_read_b128 v[226:229], v189 offset:32768
	v_exp_f32_e32 v107, v107
	v_add_f32_e32 v204, v103, v204
	v_exp_f32_e32 v108, v108
	v_add_f32_e32 v204, v104, v204
	v_exp_f32_e32 v109, v109
	v_add_f32_e32 v204, v105, v204
	s_waitcnt lgkmcnt(0)
	v_mfma_f32_32x32x64_f8f6f4 v[80:95], v[222:229], v[136:143], v[80:95]
	v_exp_f32_e32 v110, v110
	v_add_f32_e32 v204, v106, v204
	v_exp_f32_e32 v111, v111
	v_add_f32_e32 v204, v107, v204
	v_add_f32_e32 v204, v108, v204
	v_add_f32_e32 v204, v109, v204
	v_add_f32_e32 v204, v110, v204
	v_add_f32_e32 v204, v111, v204
	v_mov_b32_e32 v205, v204
	ds_read_b128 v[226:229], v192 offset:32768
	ds_read_b128 v[222:225], v191 offset:32768
	s_nop 1
	v_permlane32_swap_b32_e32 v204, v205
	v_cvt_pk_bf16_f32 v206, v112, v113
	v_cvt_pk_bf16_f32 v207, v114, v115
	v_cvt_pk_bf16_f32 v208, v116, v117
	v_cvt_pk_bf16_f32 v209, v118, v119
	v_cvt_pk_bf16_f32 v210, v120, v121
	v_cvt_pk_bf16_f32 v211, v122, v123
	s_waitcnt lgkmcnt(0)
	v_mfma_f32_32x32x64_f8f6f4 v[64:79], v[222:229], v[144:151], v[64:79]
	v_cvt_pk_bf16_f32 v212, v124, v125
	v_cvt_pk_bf16_f32 v213, v126, v127
	v_cvt_pk_bf16_f32 v214, v96, v97
	v_cvt_pk_bf16_f32 v215, v98, v99
	v_cvt_pk_bf16_f32 v216, v100, v101
	v_cvt_pk_bf16_f32 v217, v102, v103
	v_cvt_pk_bf16_f32 v218, v104, v105
	v_cvt_pk_bf16_f32 v219, v106, v107
	v_cvt_pk_bf16_f32 v220, v108, v109
	v_cvt_pk_bf16_f32 v221, v110, v111
	s_nop 0
	ds_read_b128 v[222:225], v191 offset:40960
	ds_read_b128 v[226:229], v193 offset:32768
	s_waitcnt lgkmcnt(0)
	v_mfma_f32_32x32x64_f8f6f4 v[80:95], v[222:229], v[144:151], v[80:95]
	ds_read_b64_tr_b16 v[222:223], v199 offset:0
	ds_read_b64_tr_b16 v[224:225], v199 offset:0x800
	ds_read_b64_tr_b16 v[226:227], v199 offset:0x1000
	ds_read_b64_tr_b16 v[228:229], v199 offset:0x1800
	ds_read_b64_tr_b16 v[230:231], v199 offset:0x2000
	ds_read_b64_tr_b16 v[232:233], v199 offset:0x2800
	ds_read_b64_tr_b16 v[234:235], v199 offset:0x3000
	ds_read_b64_tr_b16 v[236:237], v199 offset:0x3800
	v_max_f32_e32 v242, v65, v65
	v_max_f32_e32 v243, v64, v64
	v_max_f32_e32 v242, v243, v242
	v_max3_f32 v242, v242, v66, v67
	v_max3_f32 v242, v242, v68, v69
	v_max3_f32 v242, v242, v70, v71
	v_max3_f32 v242, v242, v72, v73
	v_max3_f32 v242, v242, v74, v75
	s_waitcnt lgkmcnt(0)
	s_nop 0
	v_mfma_f32_32x32x16_bf16 v[0:15], v[206:209], v[222:225], v[0:15]
	v_max3_f32 v242, v242, v76, v77
	v_max3_f32 v242, v242, v78, v79
	v_max3_f32 v242, v242, v80, v81
	v_max3_f32 v242, v242, v82, v83
	v_max3_f32 v242, v242, v84, v85
	ds_read_b64_tr_b16 v[222:223], v199 offset:0x200
	ds_read_b64_tr_b16 v[224:225], v199 offset:0xa00
	v_mfma_f32_32x32x16_bf16 v[0:15], v[210:213], v[226:229], v[0:15]
	v_max3_f32 v242, v242, v86, v87
	v_max3_f32 v242, v242, v88, v89
	v_max3_f32 v242, v242, v90, v91
	v_max3_f32 v242, v242, v92, v93
	v_max3_f32 v242, v242, v94, v95
	ds_read_b64_tr_b16 v[226:227], v199 offset:0x1200
	ds_read_b64_tr_b16 v[228:229], v199 offset:0x1a00
	v_mfma_f32_32x32x16_bf16 v[0:15], v[214:217], v[230:233], v[0:15]
	v_mov_b32_e32 v243, v242
	s_nop 1
	v_permlane32_swap_b32_e32 v242, v243
	ds_read_b64_tr_b16 v[230:231], v199 offset:0x2200
	ds_read_b64_tr_b16 v[232:233], v199 offset:0x2a00
	v_mfma_f32_32x32x16_bf16 v[0:15], v[218:221], v[234:237], v[0:15]
	v_max_f32_e32 v243, v243, v243
	v_max_f32_e32 v242, v242, v242
	v_max_f32_e32 v242, v242, v243
	v_sub_f32_e32 v243, v242, v195
	v_cmp_ge_f32_e32 vcc, s93, v243
	ds_read_b64_tr_b16 v[234:235], v199 offset:0x3200
	ds_read_b64_tr_b16 v[236:237], v199 offset:0x3a00
	v_max_f32_e32 v243, v195, v195
	v_max_f32_e32 v243, v243, v242
	v_sub_f32_e32 v242, v195, v243
	v_mul_f32_e32 v242, 0x3dd53b94, v242
	v_exp_f32_e32 v242, v242
	s_cmp_eq_u64 vcc, exec
	s_cselect_b64 s[6:7], -1, 0
	s_waitcnt lgkmcnt(0)
	v_mfma_f32_32x32x16_bf16 v[48:63], v[206:209], v[222:225], v[48:63]
	v_cndmask_b32_e64 v242, v242, 1.0, s[6:7]
	v_cmp_gt_f32_e32 vcc, 1.0, v242
	v_cndmask_b32_e64 v195, v243, v195, s[6:7]
	v_mul_f32_e32 v244, 0xbdd53b94, v195
	v_mov_b32_e32 v243, v244
	ds_read_b64_tr_b16 v[222:223], v199 offset:0x400
	ds_read_b64_tr_b16 v[224:225], v199 offset:0xc00
	v_mfma_f32_32x32x16_bf16 v[48:63], v[210:213], v[226:229], v[48:63]
	v_fmamk_f32 v64, v64, 0x3dd53b94, v244
	v_fmamk_f32 v65, v65, 0x3dd53b94, v244
	v_fmamk_f32 v66, v66, 0x3dd53b94, v244
	v_fmamk_f32 v67, v67, 0x3dd53b94, v244
	v_fmamk_f32 v68, v68, 0x3dd53b94, v244
	ds_read_b64_tr_b16 v[226:227], v199 offset:0x1400
	ds_read_b64_tr_b16 v[228:229], v199 offset:0x1c00
	v_mfma_f32_32x32x16_bf16 v[48:63], v[214:217], v[230:233], v[48:63]
	v_fmamk_f32 v69, v69, 0x3dd53b94, v244
	v_fmamk_f32 v70, v70, 0x3dd53b94, v244
	v_fmamk_f32 v71, v71, 0x3dd53b94, v244
	v_fmamk_f32 v72, v72, 0x3dd53b94, v244
	v_fmamk_f32 v73, v73, 0x3dd53b94, v244
	ds_read_b64_tr_b16 v[230:231], v199 offset:0x2400
	ds_read_b64_tr_b16 v[232:233], v199 offset:0x2c00
	v_mfma_f32_32x32x16_bf16 v[48:63], v[218:221], v[234:237], v[48:63]
	v_fmamk_f32 v74, v74, 0x3dd53b94, v244
	v_fmamk_f32 v75, v75, 0x3dd53b94, v244
	v_fmamk_f32 v76, v76, 0x3dd53b94, v244
	v_fmamk_f32 v77, v77, 0x3dd53b94, v244
	v_fmamk_f32 v78, v78, 0x3dd53b94, v244
	ds_read_b64_tr_b16 v[234:235], v199 offset:0x3400
	ds_read_b64_tr_b16 v[236:237], v199 offset:0x3c00
	v_fmac_f32_e32 v243, 0x3dd53b94, v79
	v_exp_f32_e32 v64, v64
	v_exp_f32_e32 v65, v65
	v_exp_f32_e32 v66, v66
	s_waitcnt lgkmcnt(0)
	v_mfma_f32_32x32x16_bf16 v[32:47], v[206:209], v[222:225], v[32:47]
	v_exp_f32_e32 v67, v67
	v_exp_f32_e32 v68, v68
	ds_read_b64_tr_b16 v[222:223], v199 offset:0x600
	ds_read_b64_tr_b16 v[224:225], v199 offset:0xe00
	v_mfma_f32_32x32x16_bf16 v[32:47], v[210:213], v[226:229], v[32:47]
	v_exp_f32_e32 v69, v69
	v_exp_f32_e32 v70, v70
	ds_read_b64_tr_b16 v[226:227], v199 offset:0x1600
	ds_read_b64_tr_b16 v[228:229], v199 offset:0x1e00
	v_mfma_f32_32x32x16_bf16 v[32:47], v[214:217], v[230:233], v[32:47]
	v_exp_f32_e32 v71, v71
	v_exp_f32_e32 v72, v72
	ds_read_b64_tr_b16 v[230:231], v199 offset:0x2600
	ds_read_b64_tr_b16 v[232:233], v199 offset:0x2e00
	v_mfma_f32_32x32x16_bf16 v[32:47], v[218:221], v[234:237], v[32:47]
	v_exp_f32_e32 v73, v73
	v_exp_f32_e32 v74, v74
	ds_read_b64_tr_b16 v[234:235], v199 offset:0x3600
	ds_read_b64_tr_b16 v[236:237], v199 offset:0x3e00
	v_exp_f32_e32 v75, v75
	v_exp_f32_e32 v76, v76
	v_exp_f32_e32 v77, v77
	v_exp_f32_e32 v78, v78
	s_waitcnt lgkmcnt(0)
	v_mfma_f32_32x32x16_bf16 v[16:31], v[206:209], v[222:225], v[16:31]
	v_exp_f32_e32 v79, v243
	v_pk_fma_f32 v[94:95], v[94:95], s[54:55], v[244:245] op_sel_hi:[1,0,0]
	v_mfma_f32_32x32x16_bf16 v[16:31], v[210:213], v[226:229], v[16:31]
	v_pk_fma_f32 v[92:93], v[92:93], s[54:55], v[244:245] op_sel_hi:[1,0,0]
	v_pk_fma_f32 v[90:91], v[90:91], s[54:55], v[244:245] op_sel_hi:[1,0,0]
	v_mfma_f32_32x32x16_bf16 v[16:31], v[214:217], v[230:233], v[16:31]
	v_pk_fma_f32 v[88:89], v[88:89], s[54:55], v[244:245] op_sel_hi:[1,0,0]
	v_pk_fma_f32 v[86:87], v[86:87], s[54:55], v[244:245] op_sel_hi:[1,0,0]
	v_mfma_f32_32x32x16_bf16 v[16:31], v[218:221], v[234:237], v[16:31]
	v_pk_fma_f32 v[84:85], v[84:85], s[54:55], v[244:245] op_sel_hi:[1,0,0]
	v_pk_fma_f32 v[82:83], v[82:83], s[54:55], v[244:245] op_sel_hi:[1,0,0]
	v_pk_fma_f32 v[80:81], v[80:81], s[54:55], v[244:245] op_sel_hi:[1,0,0]
	v_mov_b32_e32 v206, v242
	s_cbranch_vccz .Latt0_nrB
	s_nop 7
	s_nop 7
	s_and_saveexec_b64 s[38:39], s[4:5]
	ds_write_b32 v197, v206 offset:128
	s_or_b64 exec, exec, s[38:39]
	s_waitcnt lgkmcnt(0)
	v_add_u32_e32 v220, s77, v196
	ds_read_b128 v[208:211], v220 offset:224
	ds_read_b128 v[212:215], v220 offset:192
	ds_read_b128 v[216:219], v220 offset:160
	ds_read_b128 v[220:223], v220 offset:128
	s_waitcnt lgkmcnt(0)
	v_pk_mul_f32 v[12:13], v[12:13], v[208:209]
	v_pk_mul_f32 v[8:9], v[8:9], v[212:213]
	v_pk_mul_f32 v[4:5], v[4:5], v[216:217]
	v_pk_mul_f32 v[14:15], v[14:15], v[210:211]
	v_pk_mul_f32 v[10:11], v[10:11], v[214:215]
	v_pk_mul_f32 v[6:7], v[6:7], v[218:219]
	v_pk_mul_f32 v[2:3], v[2:3], v[222:223]
	v_pk_mul_f32 v[0:1], v[0:1], v[220:221]
	v_pk_mul_f32 v[60:61], v[60:61], v[208:209]
	v_pk_mul_f32 v[56:57], v[56:57], v[212:213]
	v_pk_mul_f32 v[52:53], v[52:53], v[216:217]
	v_pk_mul_f32 v[62:63], v[62:63], v[210:211]
	v_pk_mul_f32 v[58:59], v[58:59], v[214:215]
	v_pk_mul_f32 v[54:55], v[54:55], v[218:219]
	v_pk_mul_f32 v[50:51], v[50:51], v[222:223]
	v_pk_mul_f32 v[48:49], v[48:49], v[220:221]
	v_pk_mul_f32 v[44:45], v[44:45], v[208:209]
	v_pk_mul_f32 v[40:41], v[40:41], v[212:213]
	v_pk_mul_f32 v[36:37], v[36:37], v[216:217]
	v_pk_mul_f32 v[46:47], v[46:47], v[210:211]
	v_pk_mul_f32 v[42:43], v[42:43], v[214:215]
	v_pk_mul_f32 v[38:39], v[38:39], v[218:219]
	v_pk_mul_f32 v[34:35], v[34:35], v[222:223]
	v_pk_mul_f32 v[32:33], v[32:33], v[220:221]
	v_pk_mul_f32 v[28:29], v[28:29], v[208:209]
	v_pk_mul_f32 v[24:25], v[24:25], v[212:213]
	v_pk_mul_f32 v[20:21], v[20:21], v[216:217]
	v_pk_mul_f32 v[30:31], v[30:31], v[210:211]
	v_pk_mul_f32 v[26:27], v[26:27], v[214:215]
	v_pk_mul_f32 v[22:23], v[22:23], v[218:219]
	v_pk_mul_f32 v[18:19], v[18:19], v[222:223]
	v_pk_mul_f32 v[16:17], v[16:17], v[220:221]

.LBB0_513:
	v_add_f32_e32 v204, 0, v112
	v_add_f32_e32 v204, v113, v204
	v_add_f32_e32 v204, v114, v204
	v_add_f32_e32 v204, v115, v204
	v_add_f32_e32 v204, v116, v204
	v_add_f32_e32 v204, v117, v204
	v_add_f32_e32 v204, v118, v204
	v_add_f32_e32 v204, v119, v204
	v_add_f32_e32 v204, v120, v204
	v_add_f32_e32 v204, v121, v204
	v_add_f32_e32 v204, v122, v204
	v_add_f32_e32 v204, v123, v204
	v_exp_f32_e32 v96, v96
	v_add_f32_e32 v204, v124, v204
	v_exp_f32_e32 v97, v97
	v_add_f32_e32 v204, v125, v204
	v_exp_f32_e32 v98, v98
	v_add_f32_e32 v204, v126, v204
	v_exp_f32_e32 v99, v99
	v_add_f32_e32 v204, v127, v204
	v_exp_f32_e32 v100, v100
	v_add_f32_e32 v204, v96, v204
	v_exp_f32_e32 v101, v101
	v_add_f32_e32 v204, v97, v204
	v_exp_f32_e32 v102, v102
	v_add_f32_e32 v204, v98, v204
	v_exp_f32_e32 v103, v103
	v_add_f32_e32 v204, v99, v204
	v_exp_f32_e32 v104, v104
	v_add_f32_e32 v204, v100, v204
	v_exp_f32_e32 v105, v105
	v_add_f32_e32 v204, v101, v204
	v_exp_f32_e32 v106, v106
	v_add_f32_e32 v204, v102, v204
	v_exp_f32_e32 v107, v107
	v_add_f32_e32 v204, v103, v204
	v_exp_f32_e32 v108, v108
	v_add_f32_e32 v204, v104, v204
	v_exp_f32_e32 v109, v109
	v_add_f32_e32 v204, v105, v204
	v_exp_f32_e32 v110, v110
	v_add_f32_e32 v204, v106, v204
	v_exp_f32_e32 v111, v111
	v_add_f32_e32 v204, v107, v204
	v_add_f32_e32 v204, v108, v204
	v_add_f32_e32 v204, v109, v204
	v_add_f32_e32 v204, v110, v204
	v_add_f32_e32 v204, v111, v204
	v_mov_b32_e32 v205, v204
	s_nop 1
	v_permlane32_swap_b32_e32 v204, v205
	v_cvt_pk_bf16_f32 v206, v112, v113
	v_cvt_pk_bf16_f32 v207, v114, v115
	v_cvt_pk_bf16_f32 v208, v116, v117
	v_cvt_pk_bf16_f32 v209, v118, v119
	v_cvt_pk_bf16_f32 v210, v120, v121
	v_cvt_pk_bf16_f32 v211, v122, v123
	v_cvt_pk_bf16_f32 v212, v124, v125
	v_cvt_pk_bf16_f32 v213, v126, v127
	v_cvt_pk_bf16_f32 v214, v96, v97
	v_cvt_pk_bf16_f32 v215, v98, v99
	v_cvt_pk_bf16_f32 v216, v100, v101
	v_cvt_pk_bf16_f32 v217, v102, v103
	v_cvt_pk_bf16_f32 v218, v104, v105
	v_cvt_pk_bf16_f32 v219, v106, v107
	v_cvt_pk_bf16_f32 v220, v108, v109
	v_cvt_pk_bf16_f32 v221, v110, v111
	s_nop 0
	ds_read_b64_tr_b16 v[222:223], v199 offset:0
	ds_read_b64_tr_b16 v[224:225], v199 offset:0x800
	ds_read_b64_tr_b16 v[226:227], v199 offset:0x1000
	ds_read_b64_tr_b16 v[228:229], v199 offset:0x1800
	ds_read_b64_tr_b16 v[230:231], v199 offset:0x2000
	ds_read_b64_tr_b16 v[232:233], v199 offset:0x2800
	ds_read_b64_tr_b16 v[234:235], v199 offset:0x3000
	ds_read_b64_tr_b16 v[236:237], v199 offset:0x3800
	s_waitcnt lgkmcnt(0)
	s_nop 0
	v_mfma_f32_32x32x16_bf16 v[0:15], v[206:209], v[222:225], v[0:15]
	ds_read_b64_tr_b16 v[222:223], v199 offset:0x200
	ds_read_b64_tr_b16 v[224:225], v199 offset:0xa00
	v_mfma_f32_32x32x16_bf16 v[0:15], v[210:213], v[226:229], v[0:15]
	ds_read_b64_tr_b16 v[226:227], v199 offset:0x1200
	ds_read_b64_tr_b16 v[228:229], v199 offset:0x1a00
	v_mfma_f32_32x32x16_bf16 v[0:15], v[214:217], v[230:233], v[0:15]
	ds_read_b64_tr_b16 v[230:231], v199 offset:0x2200
	ds_read_b64_tr_b16 v[232:233], v199 offset:0x2a00
	v_mfma_f32_32x32x16_bf16 v[0:15], v[218:221], v[234:237], v[0:15]
	ds_read_b64_tr_b16 v[234:235], v199 offset:0x3200
	ds_read_b64_tr_b16 v[236:237], v199 offset:0x3a00
	s_waitcnt lgkmcnt(0)
	v_mfma_f32_32x32x16_bf16 v[48:63], v[206:209], v[222:225], v[48:63]
	ds_read_b64_tr_b16 v[222:223], v199 offset:0x400
	ds_read_b64_tr_b16 v[224:225], v199 offset:0xc00
	v_mfma_f32_32x32x16_bf16 v[48:63], v[210:213], v[226:229], v[48:63]
	ds_read_b64_tr_b16 v[226:227], v199 offset:0x1400
	ds_read_b64_tr_b16 v[228:229], v199 offset:0x1c00
	v_mfma_f32_32x32x16_bf16 v[48:63], v[214:217], v[230:233], v[48:63]
	ds_read_b64_tr_b16 v[230:231], v199 offset:0x2400
	ds_read_b64_tr_b16 v[232:233], v199 offset:0x2c00
	v_mfma_f32_32x32x16_bf16 v[48:63], v[218:221], v[234:237], v[48:63]
	ds_read_b64_tr_b16 v[234:235], v199 offset:0x3400
	ds_read_b64_tr_b16 v[236:237], v199 offset:0x3c00
	s_waitcnt lgkmcnt(0)
	v_mfma_f32_32x32x16_bf16 v[32:47], v[206:209], v[222:225], v[32:47]
	ds_read_b64_tr_b16 v[222:223], v199 offset:0x600
	ds_read_b64_tr_b16 v[224:225], v199 offset:0xe00
	v_mfma_f32_32x32x16_bf16 v[32:47], v[210:213], v[226:229], v[32:47]
	ds_read_b64_tr_b16 v[226:227], v199 offset:0x1600
	ds_read_b64_tr_b16 v[228:229], v199 offset:0x1e00
	v_mfma_f32_32x32x16_bf16 v[32:47], v[214:217], v[230:233], v[32:47]
	ds_read_b64_tr_b16 v[230:231], v199 offset:0x2600
	ds_read_b64_tr_b16 v[232:233], v199 offset:0x2e00
	v_mfma_f32_32x32x16_bf16 v[32:47], v[218:221], v[234:237], v[32:47]
	ds_read_b64_tr_b16 v[234:235], v199 offset:0x3600
	ds_read_b64_tr_b16 v[236:237], v199 offset:0x3e00
	s_waitcnt lgkmcnt(0)
	v_mfma_f32_32x32x16_bf16 v[16:31], v[206:209], v[222:225], v[16:31]
	s_andn2_b64 vcc, exec, s[6:7]
	v_mfma_f32_32x32x16_bf16 v[16:31], v[210:213], v[226:229], v[16:31]
	v_mfma_f32_32x32x16_bf16 v[16:31], v[214:217], v[230:233], v[16:31]
	v_mfma_f32_32x32x16_bf16 v[16:31], v[218:221], v[234:237], v[16:31]
	s_cbranch_vccnz .LBB0_519
	v_max_f32_e32 v206, v65, v65
	v_max_f32_e32 v207, v64, v64
	v_max_f32_e32 v206, v207, v206
	v_max3_f32 v206, v206, v66, v67
	v_max3_f32 v206, v206, v68, v69
	v_max3_f32 v206, v206, v70, v71
	v_max3_f32 v206, v206, v72, v73
	v_max3_f32 v206, v206, v74, v75
	v_max3_f32 v206, v206, v76, v77
	v_max3_f32 v206, v206, v78, v79
	v_max3_f32 v206, v206, v80, v81
	v_max3_f32 v206, v206, v82, v83
	v_max3_f32 v206, v206, v84, v85
	v_max3_f32 v206, v206, v86, v87
	v_max3_f32 v206, v206, v88, v89
	v_max3_f32 v206, v206, v90, v91
	v_max3_f32 v206, v206, v92, v93
	v_max3_f32 v206, v206, v94, v95
	v_mov_b32_e32 v207, v206
	s_nop 1
	v_permlane32_swap_b32_e32 v206, v207
	v_max_f32_e32 v207, v207, v207
	v_max_f32_e32 v206, v206, v206
	v_max_f32_e32 v206, v206, v207
	v_sub_f32_e32 v207, v206, v195
	v_cmp_ge_f32_e32 vcc, s93, v207
	v_max_f32_e32 v207, v195, v195
	v_max_f32_e32 v207, v207, v206
	v_sub_f32_e32 v206, v195, v207
	v_mul_f32_e32 v206, 0x3dd53b94, v206
	v_exp_f32_e32 v206, v206
	s_cmp_eq_u64 vcc, exec
	s_cselect_b64 s[6:7], -1, 0
	v_cndmask_b32_e64 v206, v206, 1.0, s[6:7]
	v_cmp_gt_f32_e32 vcc, 1.0, v206
	s_cbranch_vccz .LBB0_518
	s_and_saveexec_b64 s[38:39], s[4:5]
	ds_write_b32 v197, v206 offset:128
	s_or_b64 exec, exec, s[38:39]
	s_waitcnt lgkmcnt(0)
	v_add_u32_e32 v220, s77, v196
	ds_read_b128 v[208:211], v220 offset:224
	ds_read_b128 v[212:215], v220 offset:192
	ds_read_b128 v[216:219], v220 offset:160
	ds_read_b128 v[220:223], v220 offset:128
	s_waitcnt lgkmcnt(0)
	v_pk_mul_f32 v[12:13], v[12:13], v[208:209]
	v_pk_mul_f32 v[8:9], v[8:9], v[212:213]
	v_pk_mul_f32 v[4:5], v[4:5], v[216:217]
	v_pk_mul_f32 v[14:15], v[14:15], v[210:211]
	v_pk_mul_f32 v[10:11], v[10:11], v[214:215]
	v_pk_mul_f32 v[6:7], v[6:7], v[218:219]
	v_pk_mul_f32 v[2:3], v[2:3], v[222:223]
	v_pk_mul_f32 v[0:1], v[0:1], v[220:221]
	v_pk_mul_f32 v[60:61], v[60:61], v[208:209]
	v_pk_mul_f32 v[56:57], v[56:57], v[212:213]
	v_pk_mul_f32 v[52:53], v[52:53], v[216:217]
	v_pk_mul_f32 v[62:63], v[62:63], v[210:211]
	v_pk_mul_f32 v[58:59], v[58:59], v[214:215]
	v_pk_mul_f32 v[54:55], v[54:55], v[218:219]
	v_pk_mul_f32 v[50:51], v[50:51], v[222:223]
	v_pk_mul_f32 v[48:49], v[48:49], v[220:221]
	v_pk_mul_f32 v[44:45], v[44:45], v[208:209]
	v_pk_mul_f32 v[40:41], v[40:41], v[212:213]
	v_pk_mul_f32 v[36:37], v[36:37], v[216:217]
	v_pk_mul_f32 v[46:47], v[46:47], v[210:211]
	v_pk_mul_f32 v[42:43], v[42:43], v[214:215]
	v_pk_mul_f32 v[38:39], v[38:39], v[218:219]
	v_pk_mul_f32 v[34:35], v[34:35], v[222:223]
	v_pk_mul_f32 v[32:33], v[32:33], v[220:221]
	v_pk_mul_f32 v[28:29], v[28:29], v[208:209]
	v_pk_mul_f32 v[24:25], v[24:25], v[212:213]
	v_pk_mul_f32 v[20:21], v[20:21], v[216:217]
	v_pk_mul_f32 v[30:31], v[30:31], v[210:211]
	v_pk_mul_f32 v[26:27], v[26:27], v[214:215]
	v_pk_mul_f32 v[22:23], v[22:23], v[218:219]
	v_pk_mul_f32 v[18:19], v[18:19], v[222:223]
	v_pk_mul_f32 v[16:17], v[16:17], v[220:221]
